# speedup vs baseline: 1.0120x; 1.0073x over previous
.LBB3_25:
	s_add_i32 s12, s45, s28
	s_add_i32 s2, s43, s40
	s_add_i32 s3, s12, -2
	s_cmp_lt_i32 s3, 0
	s_mov_b32 s3, m0
	s_mov_b32 m0, s2
	s_nop 0
	global_load_lds_dwordx4 v[222:223], off
	s_mov_b32 m0, s3
	s_cbranch_scc1 .LBB3_27
	s_add_i32 s48, s12, -2
	s_lshl_b32 s49, s48, 1
	s_sub_i32 s49, s35, s49
	s_cmp_ge_i32 s49, 2
	s_cbranch_scc1 .LBB3_27
	s_cmp_lt_i32 s49, 0
	s_cbranch_scc1 .Lmfill_a
	v_sub_u32_e32 v78, v219, v243
	v_cmp_le_i32_e32 vcc, 0xffffffa5, v78
	s_nop 1
	v_cndmask_b32_e32 v98, v241, v98, vcc
	v_cmp_lt_i32_e32 vcc, 0xffffff85, v78
	s_nop 1
	v_cndmask_b32_e32 v115, v241, v115, vcc
	v_cmp_le_i32_e32 vcc, 0xffffff85, v78
	s_nop 1
	v_cndmask_b32_e32 v114, v241, v114, vcc
	v_cmp_le_i32_e32 vcc, 0xffffffa6, v78
	s_nop 1
	v_cndmask_b32_e32 v99, v241, v99, vcc
	v_cmp_le_i32_e32 vcc, 0xffffff87, v78
	s_nop 1
	v_cndmask_b32_e32 v116, v241, v116, vcc
	v_cmp_le_i32_e32 vcc, 0xffffffa7, v78
	s_nop 1
	v_cndmask_b32_e32 v100, v241, v100, vcc
	v_cmp_le_i32_e32 vcc, 0xffffff88, v78
	s_nop 1
	v_cndmask_b32_e32 v117, v241, v117, vcc
	v_cmp_le_i32_e32 vcc, 0xffffffa8, v78
	s_nop 1
	v_cndmask_b32_e32 v101, v241, v101, vcc
	v_cmp_le_i32_e32 vcc, 0xffffff8d, v78
	s_nop 1
	v_cndmask_b32_e32 v118, v241, v118, vcc
	v_cmp_le_i32_e32 vcc, 0xffffffad, v78
	s_nop 1
	v_cndmask_b32_e32 v102, v241, v102, vcc
	v_cmp_le_i32_e32 vcc, 0xffffff8e, v78
	s_nop 1
	v_cndmask_b32_e32 v119, v241, v119, vcc
	v_cmp_le_i32_e32 vcc, 0xffffffae, v78
	s_nop 1
	v_cndmask_b32_e32 v103, v241, v103, vcc
	v_cmp_le_i32_e32 vcc, 0xffffff8f, v78
	s_nop 1
	v_cndmask_b32_e32 v120, v241, v120, vcc
	v_cmp_le_i32_e32 vcc, 0xffffffaf, v78
	s_nop 1
	v_cndmask_b32_e32 v104, v241, v104, vcc
	v_cmp_le_i32_e32 vcc, 0xffffff90, v78
	s_nop 1
	v_cndmask_b32_e32 v121, v241, v121, vcc
	v_cmp_le_i32_e32 vcc, 0xffffffb0, v78
	s_nop 1
	v_cndmask_b32_e32 v105, v241, v105, vcc
	v_cmp_le_i32_e32 vcc, 0xffffff95, v78
	s_nop 1
	v_cndmask_b32_e32 v122, v241, v122, vcc
	v_cmp_le_i32_e32 vcc, 0xffffffb5, v78
	s_nop 1
	v_cndmask_b32_e32 v106, v241, v106, vcc
	v_cmp_le_i32_e32 vcc, 0xffffff96, v78
	s_nop 1
	v_cndmask_b32_e32 v123, v241, v123, vcc
	v_cmp_le_i32_e32 vcc, 0xffffffb6, v78
	s_nop 1
	v_cndmask_b32_e32 v107, v241, v107, vcc
	v_cmp_le_i32_e32 vcc, 0xffffff97, v78
	s_nop 1
	v_cndmask_b32_e32 v124, v241, v124, vcc
	v_cmp_le_i32_e32 vcc, 0xffffffb7, v78
	s_nop 1
	v_cndmask_b32_e32 v108, v241, v108, vcc
	v_cmp_le_i32_e32 vcc, 0xffffff98, v78
	s_nop 1
	v_cndmask_b32_e32 v125, v241, v125, vcc
	v_cmp_le_i32_e32 vcc, 0xffffffb8, v78
	s_nop 1
	v_cndmask_b32_e32 v109, v241, v109, vcc
	v_cmp_le_i32_e32 vcc, 0xffffff9d, v78
	s_nop 1
	v_cndmask_b32_e32 v126, v241, v126, vcc
	v_cmp_le_i32_e32 vcc, 0xffffffbd, v78
	s_nop 1
	v_cndmask_b32_e32 v110, v241, v110, vcc
	v_cmp_le_i32_e32 vcc, 0xffffff9e, v78
	s_nop 1
	v_cndmask_b32_e32 v127, v241, v127, vcc
	v_cmp_le_i32_e32 vcc, 0xffffffbe, v78
	s_nop 1
	v_cndmask_b32_e32 v111, v241, v111, vcc
	v_cmp_le_i32_e32 vcc, 0xffffff9f, v78
	s_nop 1
	v_cndmask_b32_e32 v128, v241, v128, vcc
	v_cmp_le_i32_e32 vcc, 0xffffffbf, v78
	s_nop 1
	v_cndmask_b32_e32 v112, v241, v112, vcc
	v_cmp_le_i32_e32 vcc, 0xffffffa0, v78
	s_nop 1
	v_cndmask_b32_e32 v129, v241, v129, vcc
	v_cmp_le_i32_e32 vcc, 0xffffffc0, v78
	s_nop 1
	v_cndmask_b32_e32 v113, v241, v113, vcc
	s_branch .LBB3_27
.Lmfill_a:
	v_mov_b32_e32 v98, v241
	v_mov_b32_e32 v115, v241
	v_mov_b32_e32 v114, v241
	v_mov_b32_e32 v99, v241
	v_mov_b32_e32 v116, v241
	v_mov_b32_e32 v100, v241
	v_mov_b32_e32 v117, v241
	v_mov_b32_e32 v101, v241
	v_mov_b32_e32 v118, v241
	v_mov_b32_e32 v102, v241
	v_mov_b32_e32 v119, v241
	v_mov_b32_e32 v103, v241
	v_mov_b32_e32 v120, v241
	v_mov_b32_e32 v104, v241
	v_mov_b32_e32 v121, v241
	v_mov_b32_e32 v105, v241
	v_mov_b32_e32 v122, v241
	v_mov_b32_e32 v106, v241
	v_mov_b32_e32 v123, v241
	v_mov_b32_e32 v107, v241
	v_mov_b32_e32 v124, v241
	v_mov_b32_e32 v108, v241
	v_mov_b32_e32 v125, v241
	v_mov_b32_e32 v109, v241
	v_mov_b32_e32 v126, v241
	v_mov_b32_e32 v110, v241
	v_mov_b32_e32 v127, v241
	v_mov_b32_e32 v111, v241
	v_mov_b32_e32 v128, v241
	v_mov_b32_e32 v112, v241
	v_mov_b32_e32 v129, v241
	v_mov_b32_e32 v113, v241

.LBB3_36:
	s_add_i32 s12, s12, -1
	s_cmp_lt_i32 s12, 0
	s_cbranch_scc1 .LBB3_38
	s_mov_b32 s48, s12
	s_lshl_b32 s49, s48, 1
	s_sub_i32 s49, s35, s49
	s_cmp_ge_i32 s49, 2
	s_cbranch_scc1 .LBB3_38
	s_cmp_lt_i32 s49, 0
	s_cbranch_scc1 .Lmfill_b
	v_sub_u32_e32 v107, v219, v243
	v_cmp_le_i32_e32 vcc, 0xffffffe5, v107
	s_nop 1
	v_cndmask_b32_e32 v66, v241, v66, vcc
	v_cmp_lt_i32_e32 vcc, 0xffffffc5, v107
	s_nop 1
	v_cndmask_b32_e32 v83, v241, v83, vcc
	v_cmp_le_i32_e32 vcc, 0xffffffc5, v107
	s_nop 1
	v_cndmask_b32_e32 v82, v241, v82, vcc
	v_cmp_le_i32_e32 vcc, 0xffffffe6, v107
	s_nop 1
	v_cndmask_b32_e32 v67, v241, v67, vcc
	v_cmp_le_i32_e32 vcc, 0xffffffc7, v107
	s_nop 1
	v_cndmask_b32_e32 v84, v241, v84, vcc
	v_cmp_le_i32_e32 vcc, 0xffffffe7, v107
	s_nop 1
	v_cndmask_b32_e32 v68, v241, v68, vcc
	v_cmp_le_i32_e32 vcc, 0xffffffc8, v107
	s_nop 1
	v_cndmask_b32_e32 v85, v241, v85, vcc
	v_cmp_le_i32_e32 vcc, 0xffffffe8, v107
	s_nop 1
	v_cndmask_b32_e32 v69, v241, v69, vcc
	v_cmp_le_i32_e32 vcc, 0xffffffcd, v107
	s_nop 1
	v_cndmask_b32_e32 v86, v241, v86, vcc
	v_cmp_le_i32_e32 vcc, 0xffffffed, v107
	s_nop 1
	v_cndmask_b32_e32 v70, v241, v70, vcc
	v_cmp_le_i32_e32 vcc, 0xffffffce, v107
	s_nop 1
	v_cndmask_b32_e32 v87, v241, v87, vcc
	v_cmp_le_i32_e32 vcc, 0xffffffee, v107
	s_nop 1
	v_cndmask_b32_e32 v71, v241, v71, vcc
	v_cmp_le_i32_e32 vcc, 0xffffffcf, v107
	s_nop 1
	v_cndmask_b32_e32 v88, v241, v88, vcc
	v_cmp_le_i32_e32 vcc, 0xffffffef, v107
	s_nop 1
	v_cndmask_b32_e32 v72, v241, v72, vcc
	v_cmp_le_i32_e32 vcc, 0xffffffd0, v107
	s_nop 1
	v_cndmask_b32_e32 v89, v241, v89, vcc
	v_cmp_le_i32_e32 vcc, -16, v107
	s_nop 1
	v_cndmask_b32_e32 v73, v241, v73, vcc
	v_cmp_le_i32_e32 vcc, 0xffffffd5, v107
	s_nop 1
	v_cndmask_b32_e32 v90, v241, v90, vcc
	v_cmp_le_i32_e32 vcc, -11, v107
	s_nop 1
	v_cndmask_b32_e32 v74, v241, v74, vcc
	v_cmp_le_i32_e32 vcc, 0xffffffd6, v107
	s_nop 1
	v_cndmask_b32_e32 v91, v241, v91, vcc
	v_cmp_le_i32_e32 vcc, -10, v107
	s_nop 1
	v_cndmask_b32_e32 v75, v241, v75, vcc
	v_cmp_le_i32_e32 vcc, 0xffffffd7, v107
	s_nop 1
	v_cndmask_b32_e32 v92, v241, v92, vcc
	v_cmp_le_i32_e32 vcc, -9, v107
	s_nop 1
	v_cndmask_b32_e32 v76, v241, v76, vcc
	v_cmp_le_i32_e32 vcc, 0xffffffd8, v107
	s_nop 1
	v_cndmask_b32_e32 v93, v241, v93, vcc
	v_cmp_le_i32_e32 vcc, -8, v107
	s_nop 1
	v_cndmask_b32_e32 v77, v241, v77, vcc
	v_cmp_le_i32_e32 vcc, 0xffffffdd, v107
	s_nop 1
	v_cndmask_b32_e32 v94, v241, v94, vcc
	v_cmp_le_i32_e32 vcc, -3, v107
	s_nop 1
	v_cndmask_b32_e32 v78, v241, v78, vcc
	v_cmp_le_i32_e32 vcc, 0xffffffde, v107
	s_nop 1
	v_cndmask_b32_e32 v95, v241, v95, vcc
	v_cmp_le_i32_e32 vcc, -2, v107
	s_nop 1
	v_cndmask_b32_e32 v79, v241, v79, vcc
	v_cmp_le_i32_e32 vcc, 0xffffffdf, v107
	s_nop 1
	v_cndmask_b32_e32 v96, v241, v96, vcc
	v_cmp_le_i32_e32 vcc, -1, v107
	s_nop 1
	v_cndmask_b32_e32 v80, v241, v80, vcc
	v_cmp_le_i32_e32 vcc, 0xffffffe0, v107
	s_nop 1
	v_cndmask_b32_e32 v97, v241, v97, vcc
	v_cmp_le_i32_e32 vcc, 0, v107
	s_nop 1
	v_cndmask_b32_e32 v81, v241, v81, vcc
	s_branch .LBB3_38
.Lmfill_b:
	v_mov_b32_e32 v66, v241
	v_mov_b32_e32 v83, v241
	v_mov_b32_e32 v82, v241
	v_mov_b32_e32 v67, v241
	v_mov_b32_e32 v84, v241
	v_mov_b32_e32 v68, v241
	v_mov_b32_e32 v85, v241
	v_mov_b32_e32 v69, v241
	v_mov_b32_e32 v86, v241
	v_mov_b32_e32 v70, v241
	v_mov_b32_e32 v87, v241
	v_mov_b32_e32 v71, v241
	v_mov_b32_e32 v88, v241
	v_mov_b32_e32 v72, v241
	v_mov_b32_e32 v89, v241
	v_mov_b32_e32 v73, v241
	v_mov_b32_e32 v90, v241
	v_mov_b32_e32 v74, v241
	v_mov_b32_e32 v91, v241
	v_mov_b32_e32 v75, v241
	v_mov_b32_e32 v92, v241
	v_mov_b32_e32 v76, v241
	v_mov_b32_e32 v93, v241
	v_mov_b32_e32 v77, v241
	v_mov_b32_e32 v94, v241
	v_mov_b32_e32 v78, v241
	v_mov_b32_e32 v95, v241
	v_mov_b32_e32 v79, v241
	v_mov_b32_e32 v96, v241
	v_mov_b32_e32 v80, v241
	v_mov_b32_e32 v97, v241
	v_mov_b32_e32 v81, v241

	.amdhsa_kernel _Z11attn_kernelPKtS0_S0_Pt
		.amdhsa_group_segment_fixed_size 0
		.amdhsa_private_segment_fixed_size 0
		.amdhsa_kernarg_size 288
		.amdhsa_user_sgpr_count 2
		.amdhsa_user_sgpr_dispatch_ptr 0
		.amdhsa_user_sgpr_queue_ptr 0
		.amdhsa_user_sgpr_kernarg_segment_ptr 1
		.amdhsa_user_sgpr_dispatch_id 0
		.amdhsa_user_sgpr_kernarg_preload_length 0
		.amdhsa_user_sgpr_kernarg_preload_offset 0
		.amdhsa_user_sgpr_private_segment_size 0
		.amdhsa_uses_dynamic_stack 0
		.amdhsa_enable_private_segment 0
		.amdhsa_system_sgpr_workgroup_id_x 1
		.amdhsa_system_sgpr_workgroup_id_y 0
		.amdhsa_system_sgpr_workgroup_id_z 0
		.amdhsa_system_sgpr_workgroup_info 0
		.amdhsa_system_vgpr_workitem_id 0
		.amdhsa_next_free_vgpr 256
		.amdhsa_next_free_sgpr 50
		.amdhsa_accum_offset 256
		.amdhsa_reserve_vcc 1
		.amdhsa_float_round_mode_32 0
		.amdhsa_float_round_mode_16_64 0
		.amdhsa_float_denorm_mode_32 3
		.amdhsa_float_denorm_mode_16_64 3
		.amdhsa_dx10_clamp 1
		.amdhsa_ieee_mode 1
		.amdhsa_fp16_overflow 0
		.amdhsa_tg_split 0
		.amdhsa_exception_fp_ieee_invalid_op 0
		.amdhsa_exception_fp_denorm_src 0
		.amdhsa_exception_fp_ieee_div_zero 0
		.amdhsa_exception_fp_ieee_overflow 0
		.amdhsa_exception_fp_ieee_underflow 0
		.amdhsa_exception_fp_ieee_inexact 0
		.amdhsa_exception_int_div_zero 0
	.end_amdhsa_kernel

amdhsa.kernels:
  - .agpr_count:     0
    .args:
      - .actual_access:  read_only
        .address_space:  global
        .offset:         0
        .size:           8
        .value_kind:     global_buffer
      - .actual_access:  read_only
        .address_space:  global
        .offset:         8
        .size:           8
        .value_kind:     global_buffer
      - .actual_access:  read_only
        .address_space:  global
        .offset:         16
        .size:           8
        .value_kind:     global_buffer
      - .actual_access:  write_only
        .address_space:  global
        .offset:         24
        .size:           8
        .value_kind:     global_buffer
      - .actual_access:  write_only
        .address_space:  global
        .offset:         32
        .size:           8
        .value_kind:     global_buffer
      - .actual_access:  write_only
        .address_space:  global
        .offset:         40
        .size:           8
        .value_kind:     global_buffer
    .group_segment_fixed_size: 0
    .kernarg_segment_align: 8
    .kernarg_segment_size: 48
    .language:       OpenCL C
    .language_version:
      - 2
      - 0
    .max_flat_workgroup_size: 256
    .name:           _Z10cvt_kernelPKfS0_S0_PtS1_S1_
    .private_segment_fixed_size: 0
    .sgpr_count:     16
    .sgpr_spill_count: 0
    .symbol:         _Z10cvt_kernelPKfS0_S0_PtS1_S1_.kd
    .uniform_work_group_size: 1
    .uses_dynamic_stack: false
    .vgpr_count:     40
    .vgpr_spill_count: 0
    .wavefront_size: 64
  - .agpr_count:     0
    .args:
      - .address_space:  global
        .offset:         0
        .size:           8
        .value_kind:     global_buffer
      - .address_space:  global
        .offset:         8
        .size:           8
        .value_kind:     global_buffer
      - .address_space:  global
        .offset:         16
        .size:           8
        .value_kind:     global_buffer
      - .address_space:  global
        .offset:         24
        .size:           8
        .value_kind:     global_buffer
      - .address_space:  global
        .offset:         32
        .size:           8
        .value_kind:     global_buffer
      - .address_space:  global
        .offset:         40
        .size:           8
        .value_kind:     global_buffer
    .group_segment_fixed_size: 0
    .kernarg_segment_align: 8
    .kernarg_segment_size: 48
    .language:       OpenCL C
    .language_version:
      - 2
      - 0
    .max_flat_workgroup_size: 512
    .name:           _Z10kvq_kernelPKtS0_PtS1_S1_PKf
    .private_segment_fixed_size: 0
    .sgpr_count:     44
    .sgpr_spill_count: 0
    .symbol:         _Z10kvq_kernelPKtS0_PtS1_S1_PKf.kd
    .uniform_work_group_size: 1
    .uses_dynamic_stack: false
    .vgpr_count:     172
    .vgpr_spill_count: 0
    .wavefront_size: 64
  - .agpr_count:     0
    .args:
      - .address_space:  global
        .offset:         0
        .size:           8
        .value_kind:     global_buffer
      - .address_space:  global
        .offset:         8
        .size:           8
        .value_kind:     global_buffer
      - .address_space:  global
        .offset:         16
        .size:           8
        .value_kind:     global_buffer
      - .address_space:  global
        .offset:         24
        .size:           8
        .value_kind:     global_buffer
    .group_segment_fixed_size: 0
    .kernarg_segment_align: 8
    .kernarg_segment_size: 32
    .language:       OpenCL C
    .language_version:
      - 2
      - 0
    .max_flat_workgroup_size: 512
    .name:           _Z11out2_kernelPKtS0_PfPKf
    .private_segment_fixed_size: 0
    .sgpr_count:     28
    .sgpr_spill_count: 0
    .symbol:         _Z11out2_kernelPKtS0_PfPKf.kd
    .uniform_work_group_size: 1
    .uses_dynamic_stack: false
    .vgpr_count:     154
    .vgpr_spill_count: 0
    .wavefront_size: 64
  - .agpr_count:     0
    .args:
      - .address_space:  global
        .offset:         0
        .size:           8
        .value_kind:     global_buffer
      - .address_space:  global
        .offset:         8
        .size:           8
        .value_kind:     global_buffer
      - .address_space:  global
        .offset:         16
        .size:           8
        .value_kind:     global_buffer
      - .address_space:  global
        .offset:         24
        .size:           8
        .value_kind:     global_buffer
      - .offset:         32
        .size:           4
        .value_kind:     hidden_block_count_x
      - .offset:         36
        .size:           4
        .value_kind:     hidden_block_count_y
      - .offset:         40
        .size:           4
        .value_kind:     hidden_block_count_z
      - .offset:         44
        .size:           2
        .value_kind:     hidden_group_size_x
      - .offset:         46
        .size:           2
        .value_kind:     hidden_group_size_y
      - .offset:         48
        .size:           2
        .value_kind:     hidden_group_size_z
      - .offset:         50
        .size:           2
        .value_kind:     hidden_remainder_x
      - .offset:         52
        .size:           2
        .value_kind:     hidden_remainder_y
      - .offset:         54
        .size:           2
        .value_kind:     hidden_remainder_z
      - .offset:         72
        .size:           8
        .value_kind:     hidden_global_offset_x
      - .offset:         80
        .size:           8
        .value_kind:     hidden_global_offset_y
      - .offset:         88
        .size:           8
        .value_kind:     hidden_global_offset_z
      - .offset:         96
        .size:           2
        .value_kind:     hidden_grid_dims
      - .offset:         152
        .size:           4
        .value_kind:     hidden_dynamic_lds_size
    .group_segment_fixed_size: 0
    .kernarg_segment_align: 8
    .kernarg_segment_size: 288
    .language:       OpenCL C
    .language_version:
      - 2
      - 0
    .max_flat_workgroup_size: 512
    .name:           _Z11attn_kernelPKtS0_S0_Pt
    .private_segment_fixed_size: 0
    .sgpr_count:     56
    .sgpr_spill_count: 0
    .symbol:         _Z11attn_kernelPKtS0_S0_Pt.kd
    .uniform_work_group_size: 1
    .uses_dynamic_stack: false
    .vgpr_count:     256
    .vgpr_spill_count: 0
    .wavefront_size: 64
